# adds: the phase-preamble MoeOrder::next expert searches of P11/P12 use the lane-indexed prefix-table read + ballot count (was 16 dependent LDS round trips each)
# speedup vs baseline: 1.0049x; 1.0010x over previous
.LBB0_1247:
	s_or_b64 exec, exec, s[0:1]
	s_and_b64 s[0:1], s[36:37], exec
	v_lshlrev_b32_e32 v2, 4, v0
	v_and_b32_e32 v3, 32, v0
	s_cselect_b32 s64, 15, 31
	s_add_u32 s6, s94, 0x5d8a0500
	v_bitop3_b32 v2, v2, v3, 48 bitop3:0x6c
	v_lshrrev_b32_e32 v3, 5, v0
	v_lshrrev_b32_e32 v4, 1, v0
	s_addc_u32 s7, s95, 0
	v_and_b32_e32 v3, 4, v3
	v_and_b32_e32 v223, 24, v4
	v_bfe_u32 v4, v0, 2, 2
	s_add_u32 s0, s94, 0x557a0500
	v_or3_b32 v3, v3, v4, v223
	v_lshrrev_b32_e32 v4, 3, v0
	s_addc_u32 s1, s95, 0
	v_and_or_b32 v2, v0, 64, v2
	v_and_or_b32 v197, v4, 48, v236
	v_and_or_b32 v4, v4, 32, v3
	v_writelane_b32 v254, s0, 38
	s_add_u32 s60, s94, 0x4150000
	v_lshl_or_b32 v198, v4, 11, v2
	v_bfe_u32 v4, v0, 3, 25
	v_writelane_b32 v254, s1, 39
	s_addc_u32 s61, s95, 0
	v_or_b32_e32 v4, 64, v4
	s_movk_i32 s0, 0x70
	s_add_u32 s71, s94, 0x8000
	v_and_or_b32 v221, v4, s0, v236
	s_movk_i32 s0, 0x60
	s_addc_u32 s72, s95, 0
	v_and_or_b32 v3, v4, s0, v3
	s_add_u32 s74, s94, 0x577a0500
	v_lshl_or_b32 v220, v197, 11, v2
	v_lshl_or_b32 v222, v221, 11, v2
	v_lshl_or_b32 v200, v3, 11, v2
	v_lshlrev_b32_e32 v225, 1, v223
	v_and_b32_e32 v2, 0x3c0, v1
	v_and_b32_e32 v3, 32, v196
	s_addc_u32 s75, s95, 0
	v_bitop3_b32 v224, v225, v3, v2 bitop3:0x36
	s_add_i32 s2, 0, 0x20800
	v_lshlrev_b32_e32 v2, 2, v197
	v_lshlrev_b32_e32 v3, 2, v221
	v_readlane_b32 s3, v254, 33
	v_add_u32_e32 v229, s2, v2
	v_add_u32_e32 v228, s2, v3
	s_add_i32 s2, 0, 0x20a00
	s_abs_i32 s3, s3
	v_add_u32_e32 v226, s2, v3
	v_cvt_f32_u32_e32 v3, s3
	v_add_u32_e32 v227, s2, v2
	s_add_i32 s2, 0, 0x20180
	v_mov_b32_e32 v2, s2
	v_rcp_iflag_f32_e32 v3, v3
	s_waitcnt lgkmcnt(0)
	s_barrier
	v_mul_f32_e32 v3, 0x4f7ffffe, v3
	v_cvt_u32_f32_e32 v3, v3
	ds_read_b32 v2, v2
	s_sub_i32 s10, 0, s3
	v_mov_b32_e32 v199, 0
	v_readfirstlane_b32 s11, v3
	s_mul_i32 s10, s10, s11
	s_waitcnt lgkmcnt(0)
	v_readfirstlane_b32 s2, v2
	s_mul_hi_u32 s10, s11, s10
	s_abs_i32 s9, s2
	s_add_i32 s11, s11, s10
	s_mul_hi_u32 s10, s9, s11
	s_mul_i32 s10, s10, s3
	s_sub_i32 s9, s9, s10
	s_ashr_i32 s8, s2, 31
	s_sub_i32 s10, s9, s3
	s_cmp_ge_u32 s9, s3
	s_cselect_b32 s9, s10, s9
	s_sub_i32 s10, s9, s3
	s_cmp_ge_u32 s9, s3
	s_cselect_b32 s3, s10, s9
	s_xor_b32 s3, s3, s8
	s_sub_i32 s3, s3, s8
	s_sub_i32 s59, s2, s3
	s_add_i32 s3, s3, -1
	s_cmp_lt_u32 s3, 64
	s_cselect_b64 s[2:3], -1, 0
	s_and_b64 s[66:67], s[36:37], s[2:3]
	v_readlane_b32 s2, v254, 31
	v_lshlrev_b32_e32 v204, 2, v194
	v_mov_b32_e32 v205, v199
	v_readlane_b32 s3, v254, 32
	v_cmp_gt_u32_e64 s[0:1], 64, v0
	v_mov_b32_e32 v201, v199
	v_lshl_add_u64 v[202:203], s[74:75], 0, v[204:205]
	s_mov_b64 s[8:9], -1
	s_and_b64 vcc, exec, s[2:3]
	s_cbranch_vccz .LBB0_1324
	v_readlane_b32 s3, v254, 33
	s_and_b32 s2, s43, 7
	s_ashr_i32 s3, s3, 3
	s_mul_i32 s21, s3, s2
	s_ashr_i32 s2, s43, 3
	s_add_i32 s21, s21, s2
	s_and_b64 s[2:3], s[66:67], exec
	s_cselect_b32 s23, s59, 0x7fffffff
	v_readfirstlane_b32 s2, v2
	s_min_i32 s2, s2, s23
	s_cmp_gt_i32 s2, s21
	s_cselect_b64 s[10:11], -1, 0
	s_cmp_le_i32 s2, s21
	v_readfirstlane_b32 s2, v0
	s_cbranch_scc1 .LBB0_1250
	v_lshlrev_b32_e32 v2, 2, v194
	v_add_u32_e32 v2, 0x20100, v2
	ds_read_b32 v2, v2
	s_waitcnt lgkmcnt(0)
	v_cmp_ge_i32_e32 vcc, s21, v2
	s_and_b32 vcc_lo, vcc_lo, -2
	s_bcnt1_i32_b32 s34, vcc_lo
	s_mov_b32 s35, 0
	v_readlane_b32 s40, v254, 38
	v_readlane_b32 s41, v254, 39
	s_lshl_b32 s3, s34, 2
	s_add_i32 s3, s3, 0
	s_add_i32 s3, s3, 0x20100
	v_mov_b32_e32 v2, s3
	ds_read_b32 v4, v2 offset:512
	ds_read2st64_b32 v[2:3], v2 offset1:1
	s_waitcnt lgkmcnt(1)
	v_readfirstlane_b32 s3, v4
	s_add_i32 s8, s3, 0xff
	s_ashr_i32 s8, s8, 8
	s_abs_i32 s9, s8
	v_cvt_f32_u32_e32 v4, s9
	s_waitcnt lgkmcnt(0)
	v_readfirstlane_b32 s12, v2
	s_sub_i32 s16, s21, s12
	s_xor_b32 s13, s16, s8
	v_rcp_iflag_f32_e32 v2, v4
	s_ashr_i32 s14, s13, 31
	s_sub_i32 s13, 0, s9
	s_abs_i32 s12, s16
	v_mul_f32_e32 v2, 0x4f7ffffe, v2
	v_cvt_u32_f32_e32 v2, v2
	v_readfirstlane_b32 s15, v3
	v_readfirstlane_b32 s17, v2
	s_mul_i32 s13, s13, s17
	s_mul_hi_u32 s13, s17, s13
	s_add_i32 s17, s17, s13
	s_mul_hi_u32 s13, s12, s17
	s_mul_i32 s17, s13, s9
	s_sub_i32 s12, s12, s17
	s_add_i32 s18, s13, 1
	s_sub_i32 s17, s12, s9
	s_cmp_ge_u32 s12, s9
	s_cselect_b32 s13, s18, s13
	s_cselect_b32 s12, s17, s12
	s_add_i32 s17, s13, 1
	s_cmp_ge_u32 s12, s9
	s_cselect_b32 s9, s17, s13
	s_xor_b32 s9, s9, s14
	s_sub_i32 s14, s9, s14
	s_mul_i32 s8, s8, s14
	s_sub_i32 s8, s16, s8
	s_lshl_b32 s9, s8, 8
	s_lshl_b64 s[12:13], s[34:35], 23
	s_add_i32 s8, s9, s15
	s_add_u32 s16, s60, s12
	s_addc_u32 s17, s61, s13
	s_ashr_i32 s15, s14, 31
	s_lshl_b64 s[12:13], s[14:15], 19
	s_add_u32 s38, s16, s12
	s_addc_u32 s39, s17, s13
	s_sub_i32 s3, s3, s9
	s_lshl_b32 s97, s14, 7
	s_min_i32 s68, s3, 0x100
	s_andn2_b64 vcc, exec, s[10:11]
	s_cbranch_vccz .LBB0_1251
	s_branch .LBB0_1323

.LBB0_1481:
	s_mul_i32 s6, s6, s0
	s_sub_i32 s3, s3, s6
	s_sub_i32 s6, s3, s0
	s_cmp_ge_u32 s3, s0
	s_cselect_b32 s3, s6, s3
	s_sub_i32 s6, s3, s0
	s_cmp_ge_u32 s3, s0
	s_cselect_b32 s0, s6, s3
	s_xor_b32 s0, s0, s2
	s_sub_i32 s0, s0, s2
	s_sub_i32 s63, s1, s0
	s_add_i32 s0, s0, -1
	s_cmp_lt_u32 s0, 64
	s_cselect_b64 s[0:1], -1, 0
	s_and_b64 s[64:65], s[36:37], s[0:1]
	s_add_u32 s6, s94, 0x55760000
	s_addc_u32 s7, s95, 0
	s_add_u32 s24, s94, 0x659a0500
	s_addc_u32 s25, s95, 0
	s_add_u32 s0, s94, 0x5d8a0500
	v_lshlrev_b32_e32 v3, 4, v0
	v_and_b32_e32 v4, 32, v0
	v_writelane_b32 v254, s0, 38
	s_addc_u32 s0, s95, 0
	v_bitop3_b32 v3, v3, v4, 48 bitop3:0x6c
	v_lshrrev_b32_e32 v4, 5, v0
	v_lshrrev_b32_e32 v5, 1, v0
	s_add_u32 s52, s94, 0x24150000
	v_and_b32_e32 v4, 4, v4
	v_and_b32_e32 v214, 24, v5
	v_bfe_u32 v5, v0, 2, 2
	v_lshrrev_b32_e32 v6, 3, v0
	s_addc_u32 s53, s95, 0
	v_and_or_b32 v3, v0, 64, v3
	v_or3_b32 v4, v4, v5, v214
	v_and_or_b32 v5, v6, 48, v236
	s_add_u32 s84, s94, 0xa000
	v_lshl_or_b32 v198, v5, 11, v3
	v_bfe_u32 v5, v0, 3, 25
	v_writelane_b32 v254, s0, 40
	s_addc_u32 s85, s95, 0
	v_and_or_b32 v6, v6, 32, v4
	v_or_b32_e32 v5, 64, v5
	s_movk_i32 s0, 0x70
	s_add_i32 s8, s58, -1
	v_lshl_or_b32 v200, v6, 11, v3
	v_and_or_b32 v6, v5, s0, v236
	s_movk_i32 s0, 0x60
	s_and_b64 s[2:3], s[36:37], exec
	v_and_or_b32 v4, v5, s0, v4
	v_readlane_b32 s2, v254, 31
	v_lshl_or_b32 v202, v6, 11, v3
	v_lshl_or_b32 v204, v4, 11, v3
	v_lshlrev_b32_e32 v197, 1, v214
	v_and_b32_e32 v1, 0x3c0, v1
	v_and_b32_e32 v3, 32, v196
	v_mov_b32_e32 v201, 0
	v_readlane_b32 s3, v254, 32
	v_bitop3_b32 v1, v197, v3, v1 bitop3:0x36
	v_cmp_gt_u32_e64 s[0:1], 64, v0
	v_mov_b32_e32 v205, v201
	v_mov_b32_e32 v199, v201
	v_mov_b32_e32 v203, v201
	s_cselect_b32 s56, s8, 31
	s_mov_b64 s[8:9], -1
	s_and_b64 vcc, exec, s[2:3]
	s_cbranch_vccz .LBB0_1550
	v_readlane_b32 s3, v254, 33
	s_and_b32 s2, s43, 7
	s_ashr_i32 s3, s3, 3
	s_mul_i32 s59, s3, s2
	s_ashr_i32 s2, s43, 3
	s_add_i32 s59, s59, s2
	s_and_b64 s[2:3], s[64:65], exec
	s_cselect_b32 s60, s63, 0x7fffffff
	v_readfirstlane_b32 s2, v2
	s_min_i32 s2, s2, s60
	s_cmp_gt_i32 s2, s59
	s_cselect_b64 s[10:11], -1, 0
	s_cmp_le_i32 s2, s59
	v_readfirstlane_b32 s2, v0
	s_cbranch_scc1 .LBB0_1484
	v_lshlrev_b32_e32 v2, 2, v194
	v_add_u32_e32 v2, 0x20100, v2
	ds_read_b32 v2, v2
	s_waitcnt lgkmcnt(0)
	v_cmp_ge_i32_e32 vcc, s59, v2
	s_and_b32 vcc_lo, vcc_lo, -2
	s_bcnt1_i32_b32 s22, vcc_lo
	s_mov_b32 s23, 0
	s_lshl_b32 s3, s22, 2
	s_add_i32 s3, s3, 0
	s_add_i32 s3, s3, 0x20100
	v_mov_b32_e32 v2, s3
	ds_read_b32 v4, v2 offset:512
	ds_read2st64_b32 v[2:3], v2 offset1:1
	s_waitcnt lgkmcnt(1)
	v_readfirstlane_b32 s3, v4
	s_add_i32 s8, s3, 0xff
	s_ashr_i32 s8, s8, 8
	s_abs_i32 s9, s8
	v_cvt_f32_u32_e32 v4, s9
	s_waitcnt lgkmcnt(0)
	v_readfirstlane_b32 s12, v2
	s_sub_i32 s16, 0, s9
	s_sub_i32 s14, s59, s12
	v_rcp_iflag_f32_e32 v2, v4
	s_abs_i32 s12, s14
	s_xor_b32 s15, s14, s8
	s_ashr_i32 s15, s15, 31
	v_mul_f32_e32 v2, 0x4f7ffffe, v2
	v_cvt_u32_f32_e32 v2, v2
	v_readfirstlane_b32 s13, v3
	v_readfirstlane_b32 s17, v2
	s_mul_i32 s16, s16, s17
	s_mul_hi_u32 s16, s17, s16
	s_add_i32 s17, s17, s16
	s_mul_hi_u32 s16, s12, s17
	s_mul_i32 s17, s16, s9
	s_sub_i32 s12, s12, s17
	s_add_i32 s18, s16, 1
	s_sub_i32 s17, s12, s9
	s_cmp_ge_u32 s12, s9
	s_cselect_b32 s16, s18, s16
	s_cselect_b32 s12, s17, s12
	s_add_i32 s17, s16, 1
	s_cmp_ge_u32 s12, s9
	s_cselect_b32 s9, s17, s16
	s_xor_b32 s9, s9, s15
	s_sub_i32 s12, s9, s15
	s_mul_i32 s8, s8, s12
	s_sub_i32 s8, s14, s8
	s_lshl_b32 s16, s8, 8
	s_add_i32 s8, s16, s13
	s_ashr_i32 s9, s8, 31
	s_lshl_b64 s[14:15], s[8:9], 11
	v_readlane_b32 s9, v254, 38
	s_add_u32 s28, s9, s14
	v_readlane_b32 s9, v254, 40
	s_addc_u32 s29, s9, s15
	s_lshl_b64 s[14:15], s[22:23], 22
	s_add_u32 s9, s52, s14
	s_addc_u32 s17, s53, s15
	s_ashr_i32 s13, s12, 31
	s_lshl_b64 s[14:15], s[12:13], 19
	s_add_u32 s30, s9, s14
	s_addc_u32 s31, s17, s15
	s_sub_i32 s3, s3, s16
	s_lshl_b32 s20, s12, 8
	s_min_i32 s9, s3, 0x100
	s_andn2_b64 vcc, exec, s[10:11]
	s_cbranch_vccz .LBB0_1485
	s_branch .LBB0_1549
